# v30 + non-temporal hint on the read-once z / prep-output loads of chunkprep (hgrn, mlstm raw rows) and post
# speedup vs baseline: 1.0686x; 1.0055x over previous
.LBB0_1174:
	v_ashrrev_i32_e32 v36, 4, v32
	s_and_b64 vcc, exec, s[10:11]
	s_waitcnt vmcnt(0)
	v_ashrrev_i32_e32 v37, 31, v36
	v_and_b32_e32 v24, 0xf0, v34
	s_waitcnt lgkmcnt(0)
	s_barrier
	s_cbranch_vccz .LBB0_1176
	s_ashr_i32 s4, s93, 8
	s_ashr_i32 s5, s4, 31
	s_lshl_b32 s6, s93, 5
	s_lshl_b64 s[4:5], s[4:5], 11
	s_and_b32 s6, s6, 0x7e0
	s_or_b32 s4, s4, s6
	v_lshl_add_u64 v[0:1], s[4:5], 0, v[36:37]
	v_mov_b64_e32 v[2:3], s[86:87]
	v_mad_u64_u32 v[2:3], s[4:5], v0, s1, v[2:3]
	s_lshl_b32 s4, s93, 2
	v_mad_i32_i24 v3, v1, s1, v3
	s_and_b32 s34, s4, 0x300
	v_lshl_add_u64 v[0:1], v[2:3], 0, s[34:35]
	v_mov_b32_e32 v25, v65
	v_lshl_add_u64 v[0:1], v[0:1], 0, v[24:25]
	s_mov_b64 s[4:5], 0x48000e00
	v_lshl_add_u64 v[2:3], v[0:1], 0, s[4:5]
	v_add_co_u32_e32 v0, vcc, 0x48000000, v0
	s_nop 1
	v_addc_co_u32_e32 v1, vcc, 0, v1, vcc
	global_load_dwordx4 v[12:15], v[0:1], off offset:3584 nt
	global_load_dwordx4 v[4:7], v[2:3], off offset:1024 nt
	s_nop 0
	global_load_dwordx4 v[0:3], v[2:3], off offset:2048 nt
	s_branch .LBB0_1177

.LBB0_1192:
	s_waitcnt vmcnt(4)
	v_lshlrev_b32_e32 v48, 16, v4
	v_mul_f32_e32 v48, 0xbfb8aa3b, v48
	v_exp_f32_e32 v48, v48
	s_cmp_lt_i32 s20, s32
	s_cselect_b32 s12, s20, -1
	s_and_b32 s13, s18, 0x180
	v_lshl_add_u32 v16, s13, 2, v58
	ds_read_b128 v[20:23], v16 offset:56320
	ds_read_b128 v[16:19], v16 offset:56336
	v_add_f32_e32 v48, 1.0, v48
	v_rcp_f32_e32 v71, v48
	s_mov_b32 s13, 0x3f317217
	s_waitcnt lgkmcnt(1)
	v_sub_f32_e32 v72, 1.0, v20
	s_mov_b32 s14, 0x7f800000
	v_fma_f32 v20, v72, v71, v20
	v_max_f32_e32 v20, 0x2081cea, v20
	v_cmp_gt_f32_e32 vcc, s28, v20
	v_and_b32_e32 v49, 0xffff0000, v4
	v_sub_f32_e32 v78, 1.0, v21
	v_cndmask_b32_e64 v48, 0, 32, vcc
	v_ldexp_f32 v20, v20, v48
	v_log_f32_e32 v20, v20
	v_lshlrev_b32_e32 v50, 16, v5
	v_sub_f32_e32 v77, 1.0, v22
	v_and_b32_e32 v51, 0xffff0000, v5
	v_mul_f32_e32 v48, 0x3f317217, v20
	v_fma_f32 v48, v20, s13, -v48
	v_fmac_f32_e32 v48, 0x3377d1cf, v20
	v_fmac_f32_e32 v48, 0x3f317217, v20
	v_cmp_lt_f32_e64 s[56:57], |v20|, s14
	v_sub_f32_e32 v75, 1.0, v23
	v_lshlrev_b32_e32 v53, 16, v6
	v_cndmask_b32_e64 v20, v20, v48, s[56:57]
	v_cndmask_b32_e32 v48, 0, v219, vcc
	v_sub_f32_e32 v20, v20, v48
	v_mul_f32_e32 v48, 0xbfb8aa3b, v49
	v_exp_f32_e32 v48, v48
	s_waitcnt lgkmcnt(0)
	v_sub_f32_e32 v49, 1.0, v16
	v_and_b32_e32 v55, 0xffff0000, v6
	v_lshlrev_b32_e32 v52, 16, v7
	v_add_f32_e32 v48, 1.0, v48
	v_rcp_f32_e32 v73, v48
	v_mul_f32_e32 v52, 0xbfb8aa3b, v52
	v_exp_f32_e32 v52, v52
	v_and_b32_e32 v54, 0xffff0000, v7
	v_fma_f32 v21, v78, v73, v21
	v_max_f32_e32 v21, 0x2081cea, v21
	v_cmp_gt_f32_e32 vcc, s28, v21
	v_add_f32_e32 v52, 1.0, v52
	v_rcp_f32_e32 v52, v52
	v_cndmask_b32_e64 v48, 0, 32, vcc
	v_ldexp_f32 v21, v21, v48
	v_log_f32_e32 v21, v21
	v_mul_f32_e32 v54, 0xbfb8aa3b, v54
	v_exp_f32_e32 v54, v54
	s_cmp_lt_i32 s12, 0
	v_mul_f32_e32 v48, 0x3f317217, v21
	v_fma_f32 v48, v21, s13, -v48
	v_fmac_f32_e32 v48, 0x3377d1cf, v21
	v_fmac_f32_e32 v48, 0x3f317217, v21
	v_cmp_lt_f32_e64 s[56:57], |v21|, s14
	v_add_f32_e32 v54, 1.0, v54
	v_rcp_f32_e32 v54, v54
	v_cndmask_b32_e64 v21, v21, v48, s[56:57]
	v_cndmask_b32_e32 v48, 0, v219, vcc
	v_sub_f32_e32 v21, v21, v48
	v_mul_f32_e32 v48, 0xbfb8aa3b, v50
	v_exp_f32_e32 v48, v48
	s_nop 0
	v_add_f32_e32 v48, 1.0, v48
	v_rcp_f32_e32 v76, v48
	s_nop 0
	v_fma_f32 v22, v77, v76, v22
	v_max_f32_e32 v22, 0x2081cea, v22
	v_cmp_gt_f32_e32 vcc, s28, v22
	s_nop 1
	v_cndmask_b32_e64 v48, 0, 32, vcc
	v_ldexp_f32 v22, v22, v48
	v_log_f32_e32 v22, v22
	s_nop 0
	v_mul_f32_e32 v48, 0x3f317217, v22
	v_fma_f32 v48, v22, s13, -v48
	v_fmac_f32_e32 v48, 0x3377d1cf, v22
	v_fmac_f32_e32 v48, 0x3f317217, v22
	v_cmp_lt_f32_e64 s[56:57], |v22|, s14
	s_nop 1
	v_cndmask_b32_e64 v22, v22, v48, s[56:57]
	v_cndmask_b32_e32 v48, 0, v219, vcc
	v_sub_f32_e32 v22, v22, v48
	v_mul_f32_e32 v48, 0xbfb8aa3b, v51
	v_exp_f32_e32 v48, v48
	v_sub_f32_e32 v51, 1.0, v17
	v_add_f32_e32 v48, 1.0, v48
	v_rcp_f32_e32 v74, v48
	s_nop 0
	v_fmac_f32_e32 v23, v75, v74
	v_max_f32_e32 v23, 0x2081cea, v23
	v_cmp_gt_f32_e32 vcc, s28, v23
	s_nop 1
	v_cndmask_b32_e64 v48, 0, 32, vcc
	v_ldexp_f32 v23, v23, v48
	v_log_f32_e32 v23, v23
	s_nop 0
	v_mul_f32_e32 v48, 0x3f317217, v23
	v_fma_f32 v48, v23, s13, -v48
	v_fmac_f32_e32 v48, 0x3377d1cf, v23
	v_fmac_f32_e32 v48, 0x3f317217, v23
	v_cmp_lt_f32_e64 s[56:57], |v23|, s14
	s_nop 1
	v_cndmask_b32_e64 v23, v23, v48, s[56:57]
	v_cndmask_b32_e32 v48, 0, v219, vcc
	v_sub_f32_e32 v23, v23, v48
	v_mul_f32_e32 v48, 0xbfb8aa3b, v53
	v_exp_f32_e32 v48, v48
	s_nop 0
	v_add_f32_e32 v48, 1.0, v48
	v_rcp_f32_e32 v48, v48
	s_nop 0
	v_fma_f32 v16, v48, v49, v16
	v_max_f32_e32 v16, 0x2081cea, v16
	v_cmp_gt_f32_e32 vcc, s28, v16
	s_nop 1
	v_cndmask_b32_e64 v50, 0, 32, vcc
	v_ldexp_f32 v16, v16, v50
	v_log_f32_e32 v16, v16
	s_nop 0
	v_mul_f32_e32 v50, 0x3f317217, v16
	v_fma_f32 v50, v16, s13, -v50
	v_fmac_f32_e32 v50, 0x3377d1cf, v16
	v_fmac_f32_e32 v50, 0x3f317217, v16
	v_cmp_lt_f32_e64 s[56:57], |v16|, s14
	s_nop 1
	v_cndmask_b32_e64 v16, v16, v50, s[56:57]
	v_cndmask_b32_e32 v50, 0, v219, vcc
	v_sub_f32_e32 v16, v16, v50
	v_mul_f32_e32 v50, 0xbfb8aa3b, v55
	v_exp_f32_e32 v50, v50
	s_nop 0
	v_add_f32_e32 v50, 1.0, v50
	v_rcp_f32_e32 v50, v50
	s_nop 0
	v_fma_f32 v17, v50, v51, v17
	v_max_f32_e32 v17, 0x2081cea, v17
	v_cmp_gt_f32_e32 vcc, s28, v17
	s_nop 1
	v_cndmask_b32_e64 v53, 0, 32, vcc
	v_ldexp_f32 v17, v17, v53
	v_log_f32_e32 v17, v17
	s_nop 0
	v_mul_f32_e32 v53, 0x3f317217, v17
	v_fma_f32 v53, v17, s13, -v53
	v_fmac_f32_e32 v53, 0x3377d1cf, v17
	v_fmac_f32_e32 v53, 0x3f317217, v17
	v_cmp_lt_f32_e64 s[56:57], |v17|, s14
	s_nop 1
	v_cndmask_b32_e64 v17, v17, v53, s[56:57]
	v_cndmask_b32_e32 v53, 0, v219, vcc
	v_sub_f32_e32 v17, v17, v53
	v_sub_f32_e32 v53, 1.0, v18
	v_fma_f32 v18, v52, v53, v18
	v_max_f32_e32 v18, 0x2081cea, v18
	v_cmp_gt_f32_e32 vcc, s28, v18
	s_nop 1
	v_cndmask_b32_e64 v55, 0, 32, vcc
	v_ldexp_f32 v18, v18, v55
	v_log_f32_e32 v18, v18
	s_nop 0
	v_mul_f32_e32 v55, 0x3f317217, v18
	v_fma_f32 v55, v18, s13, -v55
	v_fmac_f32_e32 v55, 0x3377d1cf, v18
	v_fmac_f32_e32 v55, 0x3f317217, v18
	v_cmp_lt_f32_e64 s[56:57], |v18|, s14
	s_nop 1
	v_cndmask_b32_e64 v18, v18, v55, s[56:57]
	v_cndmask_b32_e32 v55, 0, v219, vcc
	v_sub_f32_e32 v18, v18, v55
	v_sub_f32_e32 v55, 1.0, v19
	v_fmac_f32_e32 v19, v54, v55
	v_max_f32_e32 v19, 0x2081cea, v19
	v_cmp_gt_f32_e32 vcc, s28, v19
	s_nop 1
	v_cndmask_b32_e64 v79, 0, 32, vcc
	v_ldexp_f32 v19, v19, v79
	v_log_f32_e32 v19, v19
	s_nop 0
	v_mul_f32_e32 v79, 0x3f317217, v19
	v_fma_f32 v79, v19, s13, -v79
	v_fmac_f32_e32 v79, 0x3377d1cf, v19
	v_fmac_f32_e32 v79, 0x3f317217, v19
	v_cmp_lt_f32_e64 s[56:57], |v19|, s14
	s_nop 1
	v_cndmask_b32_e64 v19, v19, v79, s[56:57]
	v_cndmask_b32_e32 v79, 0, v219, vcc
	v_sub_f32_e32 v19, v19, v79
	ds_write_b128 v59, v[20:23] offset:37888
	ds_write_b128 v59, v[16:19] offset:37904
	s_waitcnt vmcnt(3)
	ds_write_b16 v60, v0 offset:27648
	ds_write_b16_d16_hi v60, v0 offset:27728
	ds_write_b16 v60, v1 offset:27808
	ds_write_b16_d16_hi v60, v1 offset:27888
	ds_write_b16 v60, v2 offset:27968
	ds_write_b16_d16_hi v60, v2 offset:28048
	ds_write_b16 v60, v3 offset:28128
	ds_write_b16_d16_hi v60, v3 offset:28208
	s_cbranch_scc1 .LBB0_1194
	s_lshr_b32 s34, s12, 8
	s_lshl_b32 s13, s12, 5
	s_lshl_b64 s[14:15], s[34:35], 11
	s_and_b32 s13, s13, 0x7e0
	s_or_b32 s14, s14, s13
	v_lshl_add_u64 v[0:1], s[14:15], 0, v[36:37]
	v_mov_b64_e32 v[2:3], s[86:87]
	v_mad_u64_u32 v[2:3], s[14:15], v0, s1, v[2:3]
	s_lshl_b32 s12, s12, 2
	v_mad_i32_i24 v3, v1, s1, v3
	s_and_b32 s34, s12, 0x300
	v_lshl_add_u64 v[0:1], v[2:3], 0, s[34:35]
	v_lshl_add_u64 v[0:1], v[0:1], 0, v[64:65]
	s_mov_b64 s[12:13], 0x48000e00
	v_lshl_add_u64 v[2:3], v[0:1], 0, s[12:13]
	v_add_co_u32_e32 v0, vcc, 0x48000000, v0
	s_nop 1
	v_addc_co_u32_e32 v1, vcc, 0, v1, vcc
	global_load_dwordx4 v[8:11], v[0:1], off offset:3584 nt
	global_load_dwordx4 v[4:7], v[2:3], off offset:1024 nt
	s_nop 0
	global_load_dwordx4 v[0:3], v[2:3], off offset:2048 nt

.LBB0_1241:
	v_readlane_b32 s4, v255, 9
	v_readlane_b32 s5, v255, 10
	s_and_b64 vcc, exec, s[4:5]
	s_movk_i32 s4, 0x460
	v_cmp_gt_i32_e64 s[40:41], s4, v32
	s_cbranch_vccz .LBB0_1256
	s_bfe_u32 s12, s93, 0x20006
	s_ashr_i32 s6, s93, 8
	s_add_u32 s4, s86, 0x48000000
	s_addc_u32 s5, s87, 0
	s_lshl_b32 s7, s93, 5
	s_and_b32 s14, s7, 0x7e0
	s_ashr_i32 s7, s6, 31
	s_add_i32 s15, s14, -3
	s_lshl_b64 s[6:7], s[6:7], 11
	s_lshl_b32 s13, s12, 7
	s_and_saveexec_b64 s[8:9], s[40:41]
	s_cbranch_execz .LBB0_1246
	s_waitcnt vmcnt(3)
	v_ashrrev_i32_e32 v0, 5, v32
	v_mov_b32_e32 v64, v65
	v_add_u32_e32 v4, s15, v0
	v_mov_b32_e32 v66, v65
	v_mov_b32_e32 v67, v65
	v_mov_b64_e32 v[0:1], v[64:65]
	v_cmp_lt_i32_e32 vcc, -1, v4
	v_mov_b64_e32 v[2:3], v[66:67]
	s_and_saveexec_b64 s[10:11], vcc
	s_cbranch_execz .LBB0_1245
	v_mov_b32_e32 v5, v65
	v_lshl_add_u64 v[0:1], s[6:7], 0, v[4:5]
	v_mov_b64_e32 v[2:3], s[4:5]
	v_mad_u64_u32 v[2:3], s[18:19], v0, s1, v[2:3]
	v_lshlrev_b32_e32 v0, 6, v29
	v_mad_i32_i24 v3, v1, s1, v3
	v_and_b32_e32 v64, 0x400, v0
	v_lshl_add_u64 v[0:1], v[2:3], 0, v[64:65]
	s_lshl_b32 s34, s13, 1
	v_lshl_add_u64 v[0:1], v[0:1], 0, s[34:35]
	v_mov_b32_e32 v25, v65
	v_lshl_add_u64 v[0:1], v[0:1], 0, v[24:25]
	v_add_co_u32_e32 v0, vcc, 0x1000, v0
	s_nop 1
	v_addc_co_u32_e32 v1, vcc, 0, v1, vcc
	global_load_dwordx4 v[0:3], v[0:1], off offset:3584 nt

.LBB0_1246:
	s_or_b64 exec, exec, s[8:9]
	s_movk_i32 s8, 0x260
	v_cmp_gt_i32_e32 vcc, s8, v32
	s_and_saveexec_b64 s[8:9], vcc
	s_cbranch_execz .LBB0_1250
	s_waitcnt vmcnt(4)
	v_add_u32_e32 v4, 0x200, v32
	v_ashrrev_i32_e32 v4, 5, v4
	v_mov_b32_e32 v64, v65
	v_add_u32_e32 v8, s15, v4
	v_mov_b32_e32 v66, v65
	v_mov_b32_e32 v67, v65
	v_mov_b64_e32 v[4:5], v[64:65]
	v_cmp_lt_i32_e32 vcc, -1, v8
	v_mov_b64_e32 v[6:7], v[66:67]
	s_and_saveexec_b64 s[10:11], vcc
	s_cbranch_execz .LBB0_1249
	v_mov_b32_e32 v9, v65
	v_lshl_add_u64 v[4:5], s[6:7], 0, v[8:9]
	v_mov_b64_e32 v[6:7], s[4:5]
	v_mad_u64_u32 v[6:7], s[18:19], v4, s1, v[6:7]
	v_lshlrev_b32_e32 v4, 6, v29
	v_mad_i32_i24 v7, v5, s1, v7
	v_and_b32_e32 v64, 0x400, v4
	v_lshl_add_u64 v[4:5], v[6:7], 0, v[64:65]
	s_lshl_b32 s34, s13, 1
	v_lshl_add_u64 v[4:5], v[4:5], 0, s[34:35]
	v_mov_b32_e32 v25, v65
	v_lshl_add_u64 v[4:5], v[4:5], 0, v[24:25]
	v_add_co_u32_e32 v4, vcc, 0x1000, v4
	s_nop 1
	v_addc_co_u32_e32 v5, vcc, 0, v5, vcc
	global_load_dwordx4 v[4:7], v[4:5], off offset:3584 nt

.LBB0_1250:
	s_or_b64 exec, exec, s[8:9]
	s_movk_i32 s8, 0x60
	v_cmp_gt_i32_e32 vcc, s8, v32
	s_and_saveexec_b64 s[8:9], vcc
	s_cbranch_execz .LBB0_1254
	v_add_u32_e32 v8, 0x400, v32
	v_ashrrev_i32_e32 v8, 5, v8
	v_mov_b32_e32 v64, v65
	v_add_u32_e32 v12, s15, v8
	v_mov_b32_e32 v66, v65
	v_mov_b32_e32 v67, v65
	v_mov_b64_e32 v[8:9], v[64:65]
	v_cmp_lt_i32_e32 vcc, -1, v12
	v_mov_b64_e32 v[10:11], v[66:67]
	s_and_saveexec_b64 s[10:11], vcc
	s_cbranch_execz .LBB0_1253
	v_mov_b32_e32 v13, v65
	v_lshl_add_u64 v[8:9], s[6:7], 0, v[12:13]
	v_mov_b64_e32 v[10:11], s[4:5]
	v_mad_u64_u32 v[10:11], s[18:19], v8, s1, v[10:11]
	v_lshlrev_b32_e32 v8, 6, v29
	v_mad_i32_i24 v11, v9, s1, v11
	v_and_b32_e32 v64, 0x400, v8
	v_lshl_add_u64 v[8:9], v[10:11], 0, v[64:65]
	s_lshl_b32 s34, s13, 1
	v_lshl_add_u64 v[8:9], v[8:9], 0, s[34:35]
	v_mov_b32_e32 v25, v65
	v_lshl_add_u64 v[8:9], v[8:9], 0, v[24:25]
	v_add_co_u32_e32 v8, vcc, 0x1000, v8
	s_nop 1
	v_addc_co_u32_e32 v9, vcc, 0, v9, vcc
	global_load_dwordx4 v[8:11], v[8:9], off offset:3584 nt

.LBB0_1254:
	s_or_b64 exec, exec, s[8:9]
	s_or_b32 s6, s6, s14
	v_lshl_add_u64 v[12:13], s[6:7], 0, v[36:37]
	v_mov_b64_e32 v[14:15], s[4:5]
	v_mad_u64_u32 v[14:15], s[8:9], v12, s1, v[14:15]
	v_mad_i32_i24 v15, v13, s1, v15
	s_lshl_b32 s34, s13, 1
	v_lshl_add_u64 v[12:13], v[14:15], 0, s[34:35]
	v_mov_b32_e32 v25, v65
	v_lshl_add_u64 v[12:13], v[12:13], 0, v[24:25]
	v_add_co_u32_e32 v12, vcc, 0x2000, v12
	s_cmp_lg_u32 s82, 0
	s_nop 0
	v_addc_co_u32_e32 v13, vcc, 0, v13, vcc
	global_load_dwordx4 v[12:15], v[12:13], off offset:1536 nt
	s_cbranch_scc1 .LBB0_1256
	v_and_or_b32 v18, v29, 31, s6
	v_mov_b64_e32 v[16:17], s[4:5]
	v_mad_u64_u32 v[16:17], s[4:5], v18, s1, v[16:17]
	s_mul_i32 s4, s7, 0x5800
	s_nop 0
	v_add_u32_e32 v17, s4, v17
	s_lshl_b32 s34, s12, 1
	v_lshl_add_u64 v[16:17], v[16:17], 0, s[34:35]
	s_mov_b64 s[4:5], 0x2e00
	v_lshl_add_u64 v[18:19], v[16:17], 0, s[4:5]
	v_add_co_u32_e32 v16, vcc, 0x2000, v16
	s_nop 1
	v_addc_co_u32_e32 v17, vcc, 0, v17, vcc
	global_load_ushort v16, v[16:17], off offset:3584
	s_nop 0
	global_load_ushort v17, v[18:19], off offset:8
	s_waitcnt vmcnt(1)
	v_lshlrev_b32_e32 v39, 16, v16
	s_waitcnt vmcnt(0)
	v_lshlrev_b32_e32 v38, 16, v17

.LBB0_1268:
	s_add_i32 s60, s60, s91
	s_cmp_ge_i32 s60, s32
	s_cselect_b64 s[18:19], -1, 0
	s_cmp_lt_i32 s60, s32
	s_cselect_b32 s20, s60, -1
	s_cmp_lt_i32 s20, 0
	s_cbranch_scc1 .LBB0_1285
	s_bfe_u32 s61, s20, 0x20006
	s_lshr_b32 s34, s20, 8
	s_lshl_b32 s20, s20, 5
	s_and_b32 s63, s20, 0x7e0
	s_add_i32 s64, s63, -3
	s_lshl_b64 s[20:21], s[34:35], 11
	s_lshl_b32 s62, s61, 7
	s_and_saveexec_b64 s[22:23], s[38:39]
	s_cbranch_execz .LBB0_1276
	v_mov_b32_e32 v64, v65
	v_add_u32_e32 v12, s64, v74
	v_mov_b32_e32 v66, v65
	v_mov_b32_e32 v67, v65
	v_mov_b64_e32 v[0:1], v[64:65]
	v_cmp_lt_i32_e32 vcc, -1, v12
	v_mov_b64_e32 v[2:3], v[66:67]
	s_and_saveexec_b64 s[24:25], vcc
	s_cbranch_execz .LBB0_1272
	v_mov_b32_e32 v13, v65
	v_lshl_add_u64 v[0:1], s[20:21], 0, v[12:13]
	v_mov_b64_e32 v[2:3], s[12:13]
	v_mad_u64_u32 v[2:3], s[66:67], v0, s1, v[2:3]
	v_mad_u32_u24 v3, v1, s1, v3
	v_lshlrev_b32_e32 v64, 1, v46
	v_lshl_add_u64 v[0:1], v[2:3], 0, v[64:65]
	s_lshl_b32 s34, s62, 1
	v_lshl_add_u64 v[0:1], v[0:1], 0, s[34:35]
	v_lshlrev_b32_e32 v64, 1, v40
	v_lshl_add_u64 v[0:1], v[0:1], 0, v[64:65]
	v_add_co_u32_e32 v0, vcc, 0x1000, v0
	s_nop 1
	v_addc_co_u32_e32 v1, vcc, 0, v1, vcc
	global_load_dwordx4 v[0:3], v[0:1], off offset:3584 nt

.LBB0_1277:
	v_mov_b32_e32 v64, v65
	v_add_u32_e32 v12, s64, v75
	v_mov_b32_e32 v66, v65
	v_mov_b32_e32 v67, v65
	v_mov_b64_e32 v[4:5], v[64:65]
	v_cmp_lt_i32_e32 vcc, -1, v12
	v_mov_b64_e32 v[6:7], v[66:67]
	s_and_saveexec_b64 s[24:25], vcc
	s_cbranch_execz .LBB0_1279
	v_mov_b32_e32 v13, v65
	v_lshl_add_u64 v[4:5], s[20:21], 0, v[12:13]
	v_mov_b64_e32 v[6:7], s[12:13]
	v_mad_u64_u32 v[6:7], s[66:67], v4, s1, v[6:7]
	v_mad_u32_u24 v7, v5, s1, v7
	v_lshlrev_b32_e32 v64, 1, v46
	v_lshl_add_u64 v[4:5], v[6:7], 0, v[64:65]
	s_lshl_b32 s34, s62, 1
	v_lshl_add_u64 v[4:5], v[4:5], 0, s[34:35]
	v_lshlrev_b32_e32 v64, 1, v40
	v_lshl_add_u64 v[4:5], v[4:5], 0, v[64:65]
	v_add_co_u32_e32 v4, vcc, 0x1000, v4
	s_nop 1
	v_addc_co_u32_e32 v5, vcc, 0, v5, vcc
	global_load_dwordx4 v[4:7], v[4:5], off offset:3584 nt

.LBB0_1280:
	v_mov_b32_e32 v64, v65
	v_add_u32_e32 v12, s64, v76
	v_mov_b32_e32 v66, v65
	v_mov_b32_e32 v67, v65
	v_mov_b64_e32 v[8:9], v[64:65]
	v_cmp_lt_i32_e32 vcc, -1, v12
	v_mov_b64_e32 v[10:11], v[66:67]
	s_and_saveexec_b64 s[24:25], vcc
	s_cbranch_execz .LBB0_1282
	v_mov_b32_e32 v13, v65
	v_lshl_add_u64 v[8:9], s[20:21], 0, v[12:13]
	v_mov_b64_e32 v[10:11], s[12:13]
	v_mad_u64_u32 v[10:11], s[64:65], v8, s1, v[10:11]
	v_mad_u32_u24 v11, v9, s1, v11
	v_lshlrev_b32_e32 v64, 1, v46
	v_lshl_add_u64 v[8:9], v[10:11], 0, v[64:65]
	s_lshl_b32 s34, s62, 1
	v_lshl_add_u64 v[8:9], v[8:9], 0, s[34:35]
	v_lshlrev_b32_e32 v64, 1, v40
	v_lshl_add_u64 v[8:9], v[8:9], 0, v[64:65]
	v_add_co_u32_e32 v8, vcc, 0x1000, v8
	s_nop 1
	v_addc_co_u32_e32 v9, vcc, 0, v9, vcc
	global_load_dwordx4 v[8:11], v[8:9], off offset:3584 nt

.LBB0_1283:
	s_or_b64 exec, exec, s[22:23]
	s_or_b32 s20, s20, s63
	v_lshl_add_u64 v[12:13], s[20:21], 0, v[36:37]
	v_mov_b64_e32 v[14:15], s[12:13]
	v_mad_u64_u32 v[14:15], s[22:23], v12, s1, v[14:15]
	v_mad_i32_i24 v15, v13, s1, v15
	s_lshl_b32 s34, s62, 1
	v_lshl_add_u64 v[12:13], v[14:15], 0, s[34:35]
	v_lshlrev_b32_e32 v64, 1, v40
	v_lshl_add_u64 v[12:13], v[12:13], 0, v[64:65]
	v_add_co_u32_e32 v12, vcc, 0x2000, v12
	s_nop 1
	v_addc_co_u32_e32 v13, vcc, 0, v13, vcc
	global_load_dwordx4 v[12:15], v[12:13], off offset:1536 nt
	s_and_b64 vcc, exec, s[54:55]
	s_cbranch_vccnz .LBB0_1285
	s_waitcnt vmcnt(6)
	v_or_b32_e32 v17, s20, v28
	v_mov_b64_e32 v[26:27], s[12:13]
	v_mad_u64_u32 v[26:27], s[22:23], v17, s1, v[26:27]
	v_mov_b32_e32 v17, 0x5800
	v_mad_u32_u24 v27, s21, v17, v27
	s_lshl_b32 s34, s61, 1
	v_lshl_add_u64 v[26:27], v[26:27], 0, s[34:35]
	v_lshl_add_u64 v[38:39], v[26:27], 0, s[70:71]
	v_add_co_u32_e32 v26, vcc, 0x2000, v26
	s_nop 1
	v_addc_co_u32_e32 v27, vcc, 0, v27, vcc
	global_load_ushort v17, v[26:27], off offset:3584
	global_load_ushort v19, v[38:39], off offset:8
	s_waitcnt vmcnt(1)
	v_lshlrev_b32_e32 v39, 16, v17
	s_waitcnt vmcnt(0)
	v_lshlrev_b32_e32 v38, 16, v19

.Lpost_nomap:
	s_cmp_lt_i32 s27, 1
	s_cbranch_scc1 .LBB0_1651
	s_load_dwordx2 s[18:19], s[16:17], 0x170
	s_load_dwordx2 s[24:25], s[16:17], 0xb8
	v_readlane_b32 s38, v255, 4
	v_readlane_b32 s39, v255, 5
	v_lshlrev_b32_e32 v90, 3, v32
	s_waitcnt lgkmcnt(0)
	s_add_u32 s33, s18, 0x48000000
	s_addc_u32 s40, s19, 0
	s_add_u32 s4, s18, 0x72200000
	s_addc_u32 s5, s19, 0
	s_add_u32 s6, s18, 0x74200000
	s_addc_u32 s7, s19, 0
	s_add_u32 s8, s18, 0x76200000
	s_addc_u32 s9, s19, 0
	s_add_u32 s10, s18, 0x78200000
	s_addc_u32 s11, s19, 0
	s_add_u32 s12, s18, 0x63000000
	s_addc_u32 s13, s19, 0
	s_add_u32 s14, s18, 0x60000000
	s_addc_u32 s15, s19, 0
	s_add_u32 s20, s18, 0x6c000000
	s_addc_u32 s21, s19, 0
	s_lshl_b32 s34, s38, 9
	s_lshl_b64 s[38:39], s[34:35], 2
	v_ashrrev_i32_e32 v91, 31, v90
	s_add_u32 s24, s24, s38
	s_addc_u32 s25, s25, s39
	v_lshlrev_b64 v[24:25], 2, v[90:91]
	v_lshl_add_u64 v[4:5], s[24:25], 0, v[24:25]
	global_load_dwordx4 v[0:3], v[4:5], off nt
	s_nop 0
	global_load_dwordx4 v[4:7], v[4:5], off offset:16 nt
	s_load_dwordx4 s[44:47], s[16:17], 0x78
	s_nop 0
	s_load_dwordx2 s[16:17], s[16:17], 0x90
	v_ashrrev_i32_e32 v32, 3, v32
	v_ashrrev_i32_e32 v33, 31, v32
	v_lshlrev_b64 v[32:33], 2, v[32:33]
	s_mov_b32 s34, 0
	s_waitcnt lgkmcnt(0)
	s_add_u32 s16, s16, s38
	s_addc_u32 s17, s17, s39
	v_lshl_add_u64 v[12:13], s[16:17], 0, v[24:25]
	s_add_u32 s16, s46, s38
	s_addc_u32 s17, s47, s39
	v_lshl_add_u64 v[20:21], s[16:17], 0, v[24:25]
	s_add_u32 s16, s44, s38
	s_addc_u32 s17, s45, s39
	s_ashr_i32 s23, s22, 31
	v_lshl_add_u64 v[28:29], s[16:17], 0, v[24:25]
	s_lshl_b64 s[16:17], s[22:23], 5
	s_add_u32 s16, s20, s16
	s_addc_u32 s17, s21, s17
	v_lshl_add_u64 v[34:35], s[16:17], 0, v[32:33]
	s_mul_i32 s16, s22, 0x5800
	s_mul_hi_i32 s17, s22, 0x5800
	s_add_u32 s16, s33, s16
	s_addc_u32 s17, s40, s17
	global_load_dwordx4 v[8:11], v[12:13], off nt
	s_nop 0
	global_load_dwordx4 v[12:15], v[12:13], off offset:16 nt
	s_nop 0
	global_load_dwordx4 v[16:19], v[20:21], off nt
	s_nop 0
	global_load_dwordx4 v[20:23], v[20:21], off offset:16 nt
	s_nop 0
	global_load_dwordx4 v[24:27], v[28:29], off nt
	s_nop 0
	global_load_dwordx4 v[28:31], v[28:29], off offset:16 nt
	v_lshl_add_u64 v[94:95], s[20:21], 0, v[32:33]
	global_load_dword v92, v[34:35], off
	v_lshl_add_u64 v[34:35], v[90:91], 1, s[16:17]
	s_movk_i32 s16, 0x2000
	v_add_co_u32_e32 v36, vcc, s16, v34
	s_movk_i32 s16, 0x1000
	s_nop 0
	v_addc_co_u32_e32 v37, vcc, 0, v35, vcc
	v_add_co_u32_e32 v34, vcc, s16, v34
	s_lshl_b64 s[16:17], s[22:23], 9
	s_nop 0
	v_addc_co_u32_e32 v35, vcc, 0, v35, vcc
	global_load_dwordx4 v[60:63], v[36:37], off offset:2560 nt
	global_load_dwordx4 v[70:73], v[34:35], off offset:2560 nt
	v_lshl_add_u64 v[34:35], s[16:17], 0, v[90:91]
	v_lshlrev_b64 v[34:35], 1, v[34:35]
	v_lshl_add_u64 v[36:37], s[14:15], 0, v[34:35]
	global_load_dwordx4 v[78:81], v[36:37], off nt
	v_lshl_add_u64 v[36:37], s[12:13], 0, v[34:35]
	global_load_dwordx4 v[82:85], v[36:37], off nt
	v_lshl_add_u64 v[36:37], s[8:9], 0, v[34:35]
	global_load_dwordx4 v[66:69], v[36:37], off nt
	v_lshl_add_u64 v[36:37], s[6:7], 0, v[34:35]
	v_lshl_add_u64 v[34:35], s[4:5], 0, v[34:35]
	global_load_dwordx4 v[74:77], v[36:37], off nt
	global_load_dwordx4 v[86:89], v[34:35], off nt
	s_add_u32 s16, s18, 0x78a00000
	s_addc_u32 s17, s19, 0
	s_add_u32 s18, s18, 0x79200000
	s_addc_u32 s19, s19, 0
	s_waitcnt vmcnt(9)
	v_mov_b32_e32 v101, v26
	s_waitcnt vmcnt(8)
	v_mov_b32_e32 v97, v30
	v_mov_b32_e32 v99, v28
	v_mov_b32_e32 v93, v24
	s_branch .LBB0_1647

.LBB0_1649:
	s_andn2_b64 vcc, exec, s[24:25]
	s_cbranch_vccnz .LBB0_1646
	s_add_i32 s20, s26, s22
	s_ashr_i32 s21, s20, 31
	s_lshl_b64 s[24:25], s[20:21], 9
	v_lshl_add_u64 v[32:33], s[24:25], 0, v[90:91]
	s_mul_i32 s24, s20, 0x5800
	s_mul_hi_i32 s23, s20, 0x5800
	s_add_u32 s24, s33, s24
	s_addc_u32 s25, s40, s23
	v_lshl_add_u64 v[56:57], v[90:91], 1, s[24:25]
	v_add_co_u32_e32 v52, vcc, 0x1000, v56
	v_lshlrev_b64 v[48:49], 1, v[32:33]
	s_nop 0
	v_addc_co_u32_e32 v53, vcc, 0, v57, vcc
	v_add_co_u32_e32 v56, vcc, 0x2000, v56
	s_lshl_b64 s[24:25], s[20:21], 5
	v_lshl_add_u64 v[32:33], s[4:5], 0, v[48:49]
	v_lshl_add_u64 v[36:37], s[6:7], 0, v[48:49]
	v_lshl_add_u64 v[40:41], s[8:9], 0, v[48:49]
	v_lshl_add_u64 v[44:45], s[12:13], 0, v[48:49]
	v_lshl_add_u64 v[48:49], s[14:15], 0, v[48:49]
	v_addc_co_u32_e32 v57, vcc, 0, v57, vcc
	v_lshl_add_u64 v[102:103], v[94:95], 0, s[24:25]
	global_load_dwordx4 v[32:35], v[32:33], off nt
	s_nop 0
	global_load_dwordx4 v[36:39], v[36:37], off nt
	s_nop 0
	global_load_dwordx4 v[40:43], v[40:41], off nt
	s_nop 0
	global_load_dwordx4 v[44:47], v[44:45], off nt
	s_nop 0
	global_load_dwordx4 v[48:51], v[48:49], off nt
	s_nop 0
	global_load_dwordx4 v[52:55], v[52:53], off offset:2560 nt
	s_nop 0
	global_load_dwordx4 v[56:59], v[56:57], off offset:2560 nt
	s_nop 0
	global_load_dword v64, v[102:103], off
	s_branch .LBB0_1646
